# attention key loop: no VALU in the first three MFMA gaps after the tile barrier (row-sum adds moved to the last three gaps of the S0 chain) (v33 otherwise)
# speedup vs baseline: 1.0051x; 1.0051x over previous
.Lfa_noload_0:
	ds_read_b128 v[114:117], v130 offset:64
	ds_read_b128 v[118:121], v130 offset:96
	ds_read_b128 v[122:125], v130 offset:128
	ds_read_b128 v[132:135], v130 offset:160
	ds_read_b128 v[136:139], v130 offset:192
	ds_read_b128 v[140:143], v130 offset:224
	ds_read_b128 v[146:149], v130 offset:6720
	ds_read_b128 v[150:153], v130 offset:6752
	s_waitcnt lgkmcnt(7)
	v_mfma_f32_32x32x16_bf16 v[34:49], v[114:117], v[86:89], 0
	ds_read_b128 v[154:157], v130 offset:6784
	s_waitcnt lgkmcnt(7)
	v_mfma_f32_32x32x16_bf16 v[34:49], v[118:121], v[82:85], v[34:49]
	ds_read_b128 v[158:161], v130 offset:6816
	s_waitcnt lgkmcnt(7)
	v_mfma_f32_32x32x16_bf16 v[34:49], v[122:125], v[78:81], v[34:49]
	ds_read_b128 v[162:165], v130 offset:6848
	s_waitcnt lgkmcnt(7)
	v_mfma_f32_32x32x16_bf16 v[34:49], v[132:135], v[74:77], v[34:49]
	v_add_f32_e32 v105, v105, v50
	v_add_f32_e32 v145, v145, v51
	v_add_f32_e32 v105, v105, v52
	v_add_f32_e32 v145, v145, v53
	ds_read_b128 v[166:169], v130 offset:6880
	s_waitcnt lgkmcnt(7)
	v_mfma_f32_32x32x16_bf16 v[34:49], v[136:139], v[70:73], v[34:49]
	v_add_f32_e32 v105, v105, v54
	v_add_f32_e32 v145, v145, v55
	v_add_f32_e32 v105, v105, v56
	v_add_f32_e32 v145, v145, v57
	v_add_f32_e32 v105, v105, v58
	v_add_f32_e32 v145, v145, v59
	s_waitcnt lgkmcnt(6)
	v_mfma_f32_32x32x16_bf16 v[34:49], v[140:143], v[66:69], v[34:49]
	v_add_f32_e32 v105, v105, v60
	v_add_f32_e32 v145, v145, v61
	v_add_f32_e32 v105, v105, v62
	v_add_f32_e32 v145, v145, v63
	v_add_f32_e32 v105, v105, v64
	v_add_f32_e32 v145, v145, v65
	s_waitcnt lgkmcnt(5)
	v_mfma_f32_32x32x16_bf16 v[50:65], v[146:149], v[86:89], 0
	ds_read_b128 v[114:117], v107 offset:13376
	ds_read_b128 v[118:121], v107 offset:17984
	ds_read_b128 v[122:125], v107 offset:13408
	ds_read_b128 v[132:135], v107 offset:18016
	ds_read_b128 v[136:139], v107 offset:13440
	ds_read_b128 v[140:143], v107 offset:18048
	ds_read_b128 v[146:149], v107 offset:13472
	s_waitcnt lgkmcnt(11)
	v_mfma_f32_32x32x16_bf16 v[50:65], v[150:153], v[82:85], v[50:65]
	ds_read_b128 v[150:153], v107 offset:18080
	v_lshl_add_u64 v[112:113], v[112:113], 0, s[12:13]
	v_lshl_add_u64 v[110:111], v[110:111], 0, v[194:195]
	v_lshl_add_u64 v[108:109], v[108:109], 0, s[10:11]
	v_exp_f32_e32 v34, v34
	v_exp_f32_e32 v35, v35
	s_waitcnt lgkmcnt(11)
	v_mfma_f32_32x32x16_bf16 v[50:65], v[154:157], v[78:81], v[50:65]
	v_exp_f32_e32 v36, v36
	v_exp_f32_e32 v37, v37
	v_exp_f32_e32 v38, v38
	s_waitcnt lgkmcnt(10)
	v_mfma_f32_32x32x16_bf16 v[50:65], v[158:161], v[74:77], v[50:65]
	v_exp_f32_e32 v39, v39
	v_exp_f32_e32 v40, v40
	v_exp_f32_e32 v41, v41
	v_cvt_pk_bf16_f32 v154, v34, v35
	s_waitcnt lgkmcnt(9)
	v_mfma_f32_32x32x16_bf16 v[50:65], v[162:165], v[70:73], v[50:65]
	v_cvt_pk_bf16_f32 v155, v36, v37
	v_cvt_pk_bf16_f32 v156, v38, v39
	v_exp_f32_e32 v42, v42
	v_exp_f32_e32 v43, v43
	s_waitcnt lgkmcnt(8)
	v_mfma_f32_32x32x16_bf16 v[50:65], v[166:169], v[66:69], v[50:65]
	v_cvt_pk_bf16_f32 v157, v40, v41
	v_exp_f32_e32 v44, v44
	v_exp_f32_e32 v45, v45
	v_exp_f32_e32 v46, v46
	s_waitcnt lgkmcnt(7)
	v_mfma_f32_32x32x16_bf16 v[18:33], v[114:117], v[154:157], v[18:33]
	v_exp_f32_e32 v47, v47
	v_exp_f32_e32 v48, v48
	v_exp_f32_e32 v49, v49
	v_cvt_pk_bf16_f32 v158, v42, v43
	s_waitcnt lgkmcnt(6)
	v_mfma_f32_32x32x16_bf16 v[2:17], v[118:121], v[154:157], v[2:17]
	v_cvt_pk_bf16_f32 v159, v44, v45
	v_cvt_pk_bf16_f32 v160, v46, v47
	v_cvt_pk_bf16_f32 v161, v48, v49
	v_add_f32_e32 v105, v105, v34
	v_add_f32_e32 v145, v145, v35
	v_add_f32_e32 v105, v105, v36
	v_exp_f32_e32 v50, v50
	s_waitcnt lgkmcnt(5)
	v_mfma_f32_32x32x16_bf16 v[18:33], v[122:125], v[158:161], v[18:33]
	v_exp_f32_e32 v51, v51
	v_exp_f32_e32 v52, v52
	v_exp_f32_e32 v53, v53
	s_waitcnt lgkmcnt(4)
	v_mfma_f32_32x32x16_bf16 v[2:17], v[132:135], v[158:161], v[2:17]
	v_exp_f32_e32 v54, v54
	v_exp_f32_e32 v55, v55
	v_exp_f32_e32 v56, v56
	v_exp_f32_e32 v57, v57
	v_cvt_pk_bf16_f32 v162, v50, v51
	v_cvt_pk_bf16_f32 v163, v52, v53
	v_cvt_pk_bf16_f32 v164, v54, v55
	v_cvt_pk_bf16_f32 v165, v56, v57
	v_add_f32_e32 v145, v145, v37
	v_add_f32_e32 v105, v105, v38
	s_waitcnt lgkmcnt(3)
	v_mfma_f32_32x32x16_bf16 v[18:33], v[136:139], v[162:165], v[18:33]
	v_exp_f32_e32 v58, v58
	v_exp_f32_e32 v59, v59
	v_exp_f32_e32 v60, v60
	s_waitcnt lgkmcnt(2)
	v_mfma_f32_32x32x16_bf16 v[2:17], v[140:143], v[162:165], v[2:17]
	v_exp_f32_e32 v61, v61
	v_exp_f32_e32 v62, v62
	v_exp_f32_e32 v63, v63
	v_exp_f32_e32 v64, v64
	v_exp_f32_e32 v65, v65
	v_cvt_pk_bf16_f32 v166, v58, v59
	v_cvt_pk_bf16_f32 v167, v60, v61
	v_cvt_pk_bf16_f32 v168, v62, v63
	v_cvt_pk_bf16_f32 v169, v64, v65
	v_add_f32_e32 v145, v145, v39
	v_add_f32_e32 v105, v105, v40
	s_waitcnt lgkmcnt(1)
	v_mfma_f32_32x32x16_bf16 v[18:33], v[146:149], v[166:169], v[18:33]
	v_add_f32_e32 v145, v145, v41
	v_add_f32_e32 v105, v105, v42
	v_add_f32_e32 v145, v145, v43
	v_add_f32_e32 v105, v105, v44
	v_add_f32_e32 v145, v145, v45
	s_waitcnt lgkmcnt(0)
	v_mfma_f32_32x32x16_bf16 v[2:17], v[150:153], v[166:169], v[2:17]
	v_add_f32_e32 v105, v105, v46
	v_add_f32_e32 v145, v145, v47
	v_add_f32_e32 v105, v105, v48
	v_add_f32_e32 v145, v145, v49
	s_cmp_lt_u32 s31, s65
	s_cbranch_scc0 .Lfa_nowrite_0
	s_waitcnt vmcnt(0)
	ds_write_b128 v106, v[98:101] offset:22592
	ds_write_b128 v128, v[94:97] offset:22592
	s_cmp_lg_u32 s43, 0
	s_cbranch_scc0 .Lfa_nowrite_0
	ds_write_b128 v129, v[90:93] offset:35904

.Lfa_noload_1:
	ds_read_b128 v[114:117], v130 offset:22592
	ds_read_b128 v[118:121], v130 offset:22624
	ds_read_b128 v[122:125], v130 offset:22656
	ds_read_b128 v[132:135], v130 offset:22688
	ds_read_b128 v[136:139], v130 offset:22720
	ds_read_b128 v[140:143], v130 offset:22752
	ds_read_b128 v[146:149], v130 offset:29248
	ds_read_b128 v[150:153], v130 offset:29280
	s_waitcnt lgkmcnt(7)
	v_mfma_f32_32x32x16_bf16 v[34:49], v[114:117], v[86:89], 0
	ds_read_b128 v[154:157], v130 offset:29312
	s_waitcnt lgkmcnt(7)
	v_mfma_f32_32x32x16_bf16 v[34:49], v[118:121], v[82:85], v[34:49]
	ds_read_b128 v[158:161], v130 offset:29344
	s_waitcnt lgkmcnt(7)
	v_mfma_f32_32x32x16_bf16 v[34:49], v[122:125], v[78:81], v[34:49]
	ds_read_b128 v[162:165], v130 offset:29376
	s_waitcnt lgkmcnt(7)
	v_mfma_f32_32x32x16_bf16 v[34:49], v[132:135], v[74:77], v[34:49]
	v_add_f32_e32 v105, v105, v50
	v_add_f32_e32 v145, v145, v51
	v_add_f32_e32 v105, v105, v52
	v_add_f32_e32 v145, v145, v53
	ds_read_b128 v[166:169], v130 offset:29408
	s_waitcnt lgkmcnt(7)
	v_mfma_f32_32x32x16_bf16 v[34:49], v[136:139], v[70:73], v[34:49]
	v_add_f32_e32 v105, v105, v54
	v_add_f32_e32 v145, v145, v55
	v_add_f32_e32 v105, v105, v56
	v_add_f32_e32 v145, v145, v57
	v_add_f32_e32 v105, v105, v58
	v_add_f32_e32 v145, v145, v59
	s_waitcnt lgkmcnt(6)
	v_mfma_f32_32x32x16_bf16 v[34:49], v[140:143], v[66:69], v[34:49]
	v_add_f32_e32 v105, v105, v60
	v_add_f32_e32 v145, v145, v61
	v_add_f32_e32 v105, v105, v62
	v_add_f32_e32 v145, v145, v63
	v_add_f32_e32 v105, v105, v64
	v_add_f32_e32 v145, v145, v65
	s_waitcnt lgkmcnt(5)
	v_mfma_f32_32x32x16_bf16 v[50:65], v[146:149], v[86:89], 0
	ds_read_b128 v[114:117], v107 offset:35904
	ds_read_b128 v[118:121], v107 offset:40512
	ds_read_b128 v[122:125], v107 offset:35936
	ds_read_b128 v[132:135], v107 offset:40544
	ds_read_b128 v[136:139], v107 offset:35968
	ds_read_b128 v[140:143], v107 offset:40576
	ds_read_b128 v[146:149], v107 offset:36000
	s_waitcnt lgkmcnt(11)
	v_mfma_f32_32x32x16_bf16 v[50:65], v[150:153], v[82:85], v[50:65]
	ds_read_b128 v[150:153], v107 offset:40608
	v_lshl_add_u64 v[112:113], v[112:113], 0, s[12:13]
	v_lshl_add_u64 v[110:111], v[110:111], 0, v[194:195]
	v_lshl_add_u64 v[108:109], v[108:109], 0, s[10:11]
	v_exp_f32_e32 v34, v34
	v_exp_f32_e32 v35, v35
	s_waitcnt lgkmcnt(11)
	v_mfma_f32_32x32x16_bf16 v[50:65], v[154:157], v[78:81], v[50:65]
	v_exp_f32_e32 v36, v36
	v_exp_f32_e32 v37, v37
	v_exp_f32_e32 v38, v38
	s_waitcnt lgkmcnt(10)
	v_mfma_f32_32x32x16_bf16 v[50:65], v[158:161], v[74:77], v[50:65]
	v_exp_f32_e32 v39, v39
	v_exp_f32_e32 v40, v40
	v_exp_f32_e32 v41, v41
	v_cvt_pk_bf16_f32 v154, v34, v35
	s_waitcnt lgkmcnt(9)
	v_mfma_f32_32x32x16_bf16 v[50:65], v[162:165], v[70:73], v[50:65]
	v_cvt_pk_bf16_f32 v155, v36, v37
	v_cvt_pk_bf16_f32 v156, v38, v39
	v_exp_f32_e32 v42, v42
	v_exp_f32_e32 v43, v43
	s_waitcnt lgkmcnt(8)
	v_mfma_f32_32x32x16_bf16 v[50:65], v[166:169], v[66:69], v[50:65]
	v_cvt_pk_bf16_f32 v157, v40, v41
	v_exp_f32_e32 v44, v44
	v_exp_f32_e32 v45, v45
	v_exp_f32_e32 v46, v46
	s_waitcnt lgkmcnt(7)
	v_mfma_f32_32x32x16_bf16 v[18:33], v[114:117], v[154:157], v[18:33]
	v_exp_f32_e32 v47, v47
	v_exp_f32_e32 v48, v48
	v_exp_f32_e32 v49, v49
	v_cvt_pk_bf16_f32 v158, v42, v43
	s_waitcnt lgkmcnt(6)
	v_mfma_f32_32x32x16_bf16 v[2:17], v[118:121], v[154:157], v[2:17]
	v_cvt_pk_bf16_f32 v159, v44, v45
	v_cvt_pk_bf16_f32 v160, v46, v47
	v_cvt_pk_bf16_f32 v161, v48, v49
	v_add_f32_e32 v105, v105, v34
	v_add_f32_e32 v145, v145, v35
	v_add_f32_e32 v105, v105, v36
	v_exp_f32_e32 v50, v50
	s_waitcnt lgkmcnt(5)
	v_mfma_f32_32x32x16_bf16 v[18:33], v[122:125], v[158:161], v[18:33]
	v_exp_f32_e32 v51, v51
	v_exp_f32_e32 v52, v52
	v_exp_f32_e32 v53, v53
	s_waitcnt lgkmcnt(4)
	v_mfma_f32_32x32x16_bf16 v[2:17], v[132:135], v[158:161], v[2:17]
	v_exp_f32_e32 v54, v54
	v_exp_f32_e32 v55, v55
	v_exp_f32_e32 v56, v56
	v_exp_f32_e32 v57, v57
	v_cvt_pk_bf16_f32 v162, v50, v51
	v_cvt_pk_bf16_f32 v163, v52, v53
	v_cvt_pk_bf16_f32 v164, v54, v55
	v_cvt_pk_bf16_f32 v165, v56, v57
	v_add_f32_e32 v145, v145, v37
	v_add_f32_e32 v105, v105, v38
	s_waitcnt lgkmcnt(3)
	v_mfma_f32_32x32x16_bf16 v[18:33], v[136:139], v[162:165], v[18:33]
	v_exp_f32_e32 v58, v58
	v_exp_f32_e32 v59, v59
	v_exp_f32_e32 v60, v60
	s_waitcnt lgkmcnt(2)
	v_mfma_f32_32x32x16_bf16 v[2:17], v[140:143], v[162:165], v[2:17]
	v_exp_f32_e32 v61, v61
	v_exp_f32_e32 v62, v62
	v_exp_f32_e32 v63, v63
	v_exp_f32_e32 v64, v64
	v_exp_f32_e32 v65, v65
	v_cvt_pk_bf16_f32 v166, v58, v59
	v_cvt_pk_bf16_f32 v167, v60, v61
	v_cvt_pk_bf16_f32 v168, v62, v63
	v_cvt_pk_bf16_f32 v169, v64, v65
	v_add_f32_e32 v145, v145, v39
	v_add_f32_e32 v105, v105, v40
	s_waitcnt lgkmcnt(1)
	v_mfma_f32_32x32x16_bf16 v[18:33], v[146:149], v[166:169], v[18:33]
	v_add_f32_e32 v145, v145, v41
	v_add_f32_e32 v105, v105, v42
	v_add_f32_e32 v145, v145, v43
	v_add_f32_e32 v105, v105, v44
	v_add_f32_e32 v145, v145, v45
	s_waitcnt lgkmcnt(0)
	v_mfma_f32_32x32x16_bf16 v[2:17], v[150:153], v[166:169], v[2:17]
	v_add_f32_e32 v105, v105, v46
	v_add_f32_e32 v145, v145, v47
	v_add_f32_e32 v105, v105, v48
	v_add_f32_e32 v145, v145, v49
	s_cmp_lt_u32 s31, s65
	s_cbranch_scc0 .Lfa_nowrite_1
	s_waitcnt vmcnt(0)
	ds_write_b128 v106, v[98:101] offset:64
	ds_write_b128 v128, v[94:97] offset:64
	s_cmp_lg_u32 s43, 0
	s_cbranch_scc0 .Lfa_nowrite_1
	ds_write_b128 v129, v[90:93] offset:13376
